# nt hint also on the bf16 weight-conversion stores (written once, read a phase later)
# speedup vs baseline: 1.0119x; 1.0080x over previous
.LBB0_235:
	v_lshl_add_u64 v[12:13], v[10:11], 1, v[12:13]
	s_mov_b64 s[10:11], 0
	global_store_dwordx4 v[12:13], v[2:5], off nt
	global_store_dwordx4 v[12:13], v[6:9], off offset:16 nt
	s_barrier

.LBB0_609:
	v_lshl_add_u64 v[12:13], v[10:11], 1, v[12:13]
	s_mov_b64 s[10:11], 0
	global_store_dwordx4 v[12:13], v[2:5], off nt
	global_store_dwordx4 v[12:13], v[6:9], off offset:16 nt
	s_waitcnt vmcnt(63) expcnt(7) lgkmcnt(15)
	s_barrier

.LBB0_714:
	v_lshl_add_u64 v[12:13], v[10:11], 1, v[12:13]
	s_mov_b64 s[22:23], 0
	global_store_dwordx4 v[12:13], v[2:5], off nt
	global_store_dwordx4 v[12:13], v[6:9], off offset:16 nt
	s_waitcnt vmcnt(63) expcnt(7) lgkmcnt(15)
	s_barrier

.LBB0_1007:
	s_cmpk_gt_u32 s14, 0x41ff
	v_lshl_add_u64 v[12:13], v[10:11], 1, v[12:13]
	s_cselect_b64 s[10:11], -1, 0
	global_store_dwordx4 v[12:13], v[2:5], off nt
	global_store_dwordx4 v[12:13], v[6:9], off offset:16 nt
	s_waitcnt vmcnt(63) expcnt(7) lgkmcnt(15)
	s_barrier

.LBB0_1112:
	v_lshl_add_u64 v[12:13], v[10:11], 1, v[12:13]
	s_mov_b64 s[24:25], 0
	global_store_dwordx4 v[12:13], v[2:5], off nt
	global_store_dwordx4 v[12:13], v[6:9], off offset:16 nt
	s_barrier

.LBB0_1221:
	v_lshl_add_u64 v[12:13], v[10:11], 1, v[12:13]
	s_mov_b64 s[24:25], 0
	global_store_dwordx4 v[12:13], v[2:5], off nt
	global_store_dwordx4 v[12:13], v[6:9], off offset:16 nt
	s_waitcnt vmcnt(63) expcnt(7) lgkmcnt(15)
	s_barrier

.LBB0_1319:
	s_cmpk_gt_u32 s26, 0x49ff
	v_lshl_add_u64 v[12:13], v[10:11], 1, v[12:13]
	s_cselect_b64 s[22:23], -1, 0
	global_store_dwordx4 v[12:13], v[2:5], off nt
	global_store_dwordx4 v[12:13], v[6:9], off offset:16 nt
	s_barrier

.LBB0_1978:
	v_lshl_add_u64 v[12:13], v[10:11], 1, v[12:13]
	s_mov_b64 s[12:13], 0
	global_store_dwordx4 v[12:13], v[2:5], off nt
	global_store_dwordx4 v[12:13], v[6:9], off offset:16 nt
	s_waitcnt vmcnt(63) expcnt(7) lgkmcnt(15)
	s_barrier

.LBB0_2003:
	s_cmpk_gt_u32 s14, 0x75ff
	v_lshl_add_u64 v[12:13], v[10:11], 1, v[12:13]
	s_cselect_b64 s[10:11], -1, 0
	global_store_dwordx4 v[12:13], v[2:5], off nt
	global_store_dwordx4 v[12:13], v[6:9], off offset:16 nt
	s_waitcnt vmcnt(63) expcnt(7) lgkmcnt(15)
	s_barrier

.LBB0_2133:
	v_lshl_add_u64 v[12:13], v[10:11], 1, v[12:13]
	s_mov_b64 s[22:23], 0
	global_store_dwordx4 v[12:13], v[2:5], off nt
	global_store_dwordx4 v[12:13], v[6:9], off offset:16 nt
	s_barrier
